# baseline (speedup 1.0000x reference)
.LBB2_12:
	s_waitcnt lgkmcnt(0)
	s_mov_b32 s16, 0
	s_mov_b32 s22, s6
	s_mov_b32 s23, s7
	s_mov_b32 s17, s78
	.p2align	6
